# sel phase: dropped the zero-initialising v_mov before each pair of fp8 pack conversions (both halves are written)
# speedup vs baseline: 1.0072x; 1.0072x over previous
; __device__ __forceinline__ unsigned pk4_fp8(float a, float b, float c, float d) { unsigned w = 0u; w = __builtin_amdgcn_cvt_pk_fp8_f32(a, b, w, false); w = __builtin_amdgcn_cvt_pk_fp8_f32(c, d, w, true); return w; }
; #define LGKM_W(n) asm volatile("s_waitcnt lgkmcnt(" #n ")" ::: "memory"); SBAR()
; #define PV8_MM(dt) do { g.o[dt] = __builtin_amdgcn_mfma_f32_16x16x32_fp8_fp8(f.a[dt][0], b0, g.o[dt], 0, 0, 0); g.o[dt] = __builtin_amdgcn_mfma_f32_16x16x32_fp8_fp8(f.a[dt][1], b1, g.o[dt], 0, 0, 0); } while (0)
; template <class G> __device__ __forceinline__ void pv8_mm(G& g, const f32x4 (&s)[4], const VT8Frag& f) {
;     ...
;     unsigned pa[4];
; #pragma unroll
;     for (int T_ = 0; T_ < 4; ++T_) pa[T_] = pk4_fp8(s[T_][0], s[T_][1], s[T_][2], s[T_][3]);
;     const long b0 = (long)(((unsigned long long)pa[1] << 32) | pa[0]), b1 = (long)(((unsigned long long)pa[3] << 32) | pa[2]);
;     LGKM_W(14); PV8_MM(0); LGKM_W(12); PV8_MM(1); LGKM_W(10); PV8_MM(2); LGKM_W(8); PV8_MM(3);
;     LGKM_W(6); PV8_MM(4); LGKM_W(4); PV8_MM(5); LGKM_W(2); PV8_MM(6); LGKM_W(0); PV8_MM(7);
; template <class G> __device__ __forceinline__ void online_sm8(f32x4 (&s)[4], G& g, const float ref) {
;     ...
;     float ps = 0.f;
; #pragma unroll
;     for (int T_ = 0; T_ < 4; ++T_)
; #pragma unroll
;         for (int i = 0; i < 4; ++i) { s[T_][i] = __builtin_amdgcn_exp2f(s[T_][i]); ps += s[T_][i]; }
;     g.l += ps;
.LBB0_1797:
	v_exp_f32_e32 v18, v84
	v_exp_f32_e32 v85, v85
	v_exp_f32_e32 v114, v86
	v_exp_f32_e32 v116, v87
	v_add_f32_e32 v84, 0, v18
	v_exp_f32_e32 v86, v88
	v_add_f32_e32 v84, v84, v85
	v_exp_f32_e32 v87, v89
	v_add_f32_e32 v84, v114, v84
	v_exp_f32_e32 v88, v90
	v_add_f32_e32 v84, v116, v84
	v_exp_f32_e32 v89, v91
	v_add_f32_e32 v84, v86, v84
	v_exp_f32_e32 v90, v92
	v_add_f32_e32 v84, v87, v84
	v_exp_f32_e32 v91, v93
	v_add_f32_e32 v84, v88, v84
	v_exp_f32_e32 v92, v94
	v_add_f32_e32 v84, v89, v84
	v_exp_f32_e32 v93, v95
	v_add_f32_e32 v84, v90, v84
	v_exp_f32_e32 v94, v96
	v_add_f32_e32 v84, v91, v84
	v_exp_f32_e32 v95, v97
	v_add_f32_e32 v84, v92, v84
	v_exp_f32_e32 v96, v98
	v_add_f32_e32 v84, v93, v84
	v_exp_f32_e32 v97, v99
	v_add_f32_e32 v84, v94, v84
	v_add_f32_e32 v84, v95, v84
	v_add_f32_e32 v84, v96, v84
	v_add_f32_e32 v84, v97, v84
	v_add_f32_e32 v182, v182, v84
	v_cvt_pk_fp8_f32 v84, v18, v85
	v_cvt_pk_fp8_f32 v85, v86, v87
	v_cvt_pk_fp8_f32 v86, v90, v91
	v_cvt_pk_fp8_f32 v87, v94, v95
	s_waitcnt lgkmcnt(14)
	v_cvt_pk_fp8_f32 v84, v114, v116 op_sel:[0,0,1]
	v_cvt_pk_fp8_f32 v85, v88, v89 op_sel:[0,0,1]
	v_cvt_pk_fp8_f32 v86, v92, v93 op_sel:[0,0,1]
	v_cvt_pk_fp8_f32 v87, v96, v97 op_sel:[0,0,1]
	v_mfma_f32_16x16x32_fp8_fp8 v[48:51], v[148:149], v[84:85], v[48:51]
	s_waitcnt lgkmcnt(12)
	s_nop 0
	v_mfma_f32_16x16x32_fp8_fp8 v[48:51], v[146:147], v[86:87], v[48:51]
	v_mfma_f32_16x16x32_fp8_fp8 v[44:47], v[144:145], v[84:85], v[44:47]
	s_waitcnt lgkmcnt(10)
	v_mfma_f32_16x16x32_fp8_fp8 v[44:47], v[142:143], v[86:87], v[44:47]
	v_mfma_f32_16x16x32_fp8_fp8 v[40:43], v[140:141], v[84:85], v[40:43]
	s_waitcnt lgkmcnt(8)
	v_mfma_f32_16x16x32_fp8_fp8 v[40:43], v[136:137], v[86:87], v[40:43]
	v_mfma_f32_16x16x32_fp8_fp8 v[36:39], v[138:139], v[84:85], v[36:39]
	s_waitcnt lgkmcnt(6)
	v_mfma_f32_16x16x32_fp8_fp8 v[36:39], v[134:135], v[86:87], v[36:39]
	v_mfma_f32_16x16x32_fp8_fp8 v[32:35], v[132:133], v[84:85], v[32:35]
	s_waitcnt lgkmcnt(4)
	v_mfma_f32_16x16x32_fp8_fp8 v[32:35], v[130:131], v[86:87], v[32:35]
	v_mfma_f32_16x16x32_fp8_fp8 v[28:31], v[128:129], v[84:85], v[28:31]
	s_waitcnt lgkmcnt(2)
	v_mfma_f32_16x16x32_fp8_fp8 v[28:31], v[126:127], v[86:87], v[28:31]
	v_mfma_f32_16x16x32_fp8_fp8 v[24:27], v[124:125], v[84:85], v[24:27]
	s_waitcnt lgkmcnt(0)
	v_mfma_f32_16x16x32_fp8_fp8 v[24:27], v[120:121], v[86:87], v[24:27]
	v_mfma_f32_16x16x32_fp8_fp8 v[20:23], v[118:119], v[84:85], v[20:23]
	v_mfma_f32_16x16x32_fp8_fp8 v[20:23], v[122:123], v[86:87], v[20:23]

; __device__ __forceinline__ unsigned pk4_fp8(float a, float b, float c, float d) { unsigned w = 0u; w = __builtin_amdgcn_cvt_pk_fp8_f32(a, b, w, false); w = __builtin_amdgcn_cvt_pk_fp8_f32(c, d, w, true); return w; }
; #define LGKM_W(n) asm volatile("s_waitcnt lgkmcnt(" #n ")" ::: "memory"); SBAR()
; #define PV8_MM(dt) do { g.o[dt] = __builtin_amdgcn_mfma_f32_16x16x32_fp8_fp8(f.a[dt][0], b0, g.o[dt], 0, 0, 0); g.o[dt] = __builtin_amdgcn_mfma_f32_16x16x32_fp8_fp8(f.a[dt][1], b1, g.o[dt], 0, 0, 0); } while (0)
; template <class G> __device__ __forceinline__ void pv8_mm(G& g, const f32x4 (&s)[4], const VT8Frag& f) {
;     ...
;     unsigned pa[4];
; #pragma unroll
;     for (int T_ = 0; T_ < 4; ++T_) pa[T_] = pk4_fp8(s[T_][0], s[T_][1], s[T_][2], s[T_][3]);
;     const long b0 = (long)(((unsigned long long)pa[1] << 32) | pa[0]), b1 = (long)(((unsigned long long)pa[3] << 32) | pa[2]);
;     LGKM_W(14); PV8_MM(0); LGKM_W(12); PV8_MM(1); LGKM_W(10); PV8_MM(2); LGKM_W(8); PV8_MM(3);
;     LGKM_W(6); PV8_MM(4); LGKM_W(4); PV8_MM(5); LGKM_W(2); PV8_MM(6); LGKM_W(0); PV8_MM(7);
; template <class G> __device__ __forceinline__ void online_sm8(f32x4 (&s)[4], G& g, const float ref) {
;     ...
;     float ps = 0.f;
; #pragma unroll
;     for (int T_ = 0; T_ < 4; ++T_)
; #pragma unroll
;         for (int i = 0; i < 4; ++i) { s[T_][i] = __builtin_amdgcn_exp2f(s[T_][i]); ps += s[T_][i]; }
;     g.l += ps;
.LBB0_1808:
	v_exp_f32_e32 v18, v84
	v_exp_f32_e32 v85, v85
	v_exp_f32_e32 v114, v86
	v_exp_f32_e32 v116, v87
	v_add_f32_e32 v84, 0, v18
	v_exp_f32_e32 v86, v88
	v_add_f32_e32 v84, v84, v85
	v_exp_f32_e32 v87, v89
	v_add_f32_e32 v84, v114, v84
	v_exp_f32_e32 v88, v90
	v_add_f32_e32 v84, v116, v84
	v_exp_f32_e32 v89, v91
	v_add_f32_e32 v84, v86, v84
	v_exp_f32_e32 v90, v92
	v_add_f32_e32 v84, v87, v84
	v_exp_f32_e32 v91, v93
	v_add_f32_e32 v84, v88, v84
	v_exp_f32_e32 v92, v94
	v_add_f32_e32 v84, v89, v84
	v_exp_f32_e32 v93, v95
	v_add_f32_e32 v84, v90, v84
	v_exp_f32_e32 v94, v96
	v_add_f32_e32 v84, v91, v84
	v_exp_f32_e32 v95, v97
	v_add_f32_e32 v84, v92, v84
	v_exp_f32_e32 v96, v98
	v_add_f32_e32 v84, v93, v84
	v_exp_f32_e32 v97, v99
	v_add_f32_e32 v84, v94, v84
	v_add_f32_e32 v84, v95, v84
	v_add_f32_e32 v84, v96, v84
	v_add_f32_e32 v84, v97, v84
	v_add_f32_e32 v183, v183, v84
	v_cvt_pk_fp8_f32 v84, v18, v85
	v_cvt_pk_fp8_f32 v85, v86, v87
	v_cvt_pk_fp8_f32 v86, v90, v91
	v_cvt_pk_fp8_f32 v87, v94, v95
	s_waitcnt lgkmcnt(14)
	v_cvt_pk_fp8_f32 v84, v114, v116 op_sel:[0,0,1]
	v_cvt_pk_fp8_f32 v85, v88, v89 op_sel:[0,0,1]
	v_cvt_pk_fp8_f32 v86, v92, v93 op_sel:[0,0,1]
	v_cvt_pk_fp8_f32 v87, v96, v97 op_sel:[0,0,1]
	v_mfma_f32_16x16x32_fp8_fp8 v[80:83], v[148:149], v[84:85], v[80:83]
	s_waitcnt lgkmcnt(12)
	s_nop 0
	v_mfma_f32_16x16x32_fp8_fp8 v[80:83], v[146:147], v[86:87], v[80:83]
	v_mfma_f32_16x16x32_fp8_fp8 v[76:79], v[144:145], v[84:85], v[76:79]
	s_waitcnt lgkmcnt(10)
	v_mfma_f32_16x16x32_fp8_fp8 v[76:79], v[142:143], v[86:87], v[76:79]
	v_mfma_f32_16x16x32_fp8_fp8 v[72:75], v[140:141], v[84:85], v[72:75]
	s_waitcnt lgkmcnt(8)
	v_mfma_f32_16x16x32_fp8_fp8 v[72:75], v[136:137], v[86:87], v[72:75]
	v_mfma_f32_16x16x32_fp8_fp8 v[68:71], v[138:139], v[84:85], v[68:71]
	s_waitcnt lgkmcnt(6)
	v_mfma_f32_16x16x32_fp8_fp8 v[68:71], v[134:135], v[86:87], v[68:71]
	v_mfma_f32_16x16x32_fp8_fp8 v[64:67], v[132:133], v[84:85], v[64:67]
	s_waitcnt lgkmcnt(4)
	v_mfma_f32_16x16x32_fp8_fp8 v[64:67], v[130:131], v[86:87], v[64:67]
	v_mfma_f32_16x16x32_fp8_fp8 v[60:63], v[128:129], v[84:85], v[60:63]
	s_waitcnt lgkmcnt(2)
	v_mfma_f32_16x16x32_fp8_fp8 v[60:63], v[126:127], v[86:87], v[60:63]
	v_mfma_f32_16x16x32_fp8_fp8 v[56:59], v[124:125], v[84:85], v[56:59]
	s_waitcnt lgkmcnt(0)
	v_mfma_f32_16x16x32_fp8_fp8 v[56:59], v[120:121], v[86:87], v[56:59]
	v_mfma_f32_16x16x32_fp8_fp8 v[52:55], v[118:119], v[84:85], v[52:55]
	v_mfma_f32_16x16x32_fp8_fp8 v[52:55], v[122:123], v[86:87], v[52:55]
